# waitcnt placement: phase D lru arm waits for the gate row after all nine loads are issued instead of between the third and fourth
# speedup vs baseline: 1.1950x; 1.0036x over previous
.LBB0_642:
	s_andn2_saveexec_b64 s[72:73], s[72:73]
	s_cbranch_execz .LBB0_639
	v_mad_i64_i32 v[0:1], s[40:41], v58, s95, v[56:57]
	global_load_dwordx4 v[0:3], v[0:1], off offset:2048
	v_lshl_add_u64 v[12:13], v[48:49], 0, v[6:7]
	v_lshl_add_u64 v[16:17], v[50:51], 0, v[6:7]
	global_load_dwordx4 v[4:7], v[12:13], off
	global_load_dwordx4 v[8:11], v[16:17], off
	v_add_co_u32_e32 v12, vcc, s42, v12
	v_addc_co_u32_e32 v13, vcc, 0, v13, vcc
	global_load_dwordx4 v[12:15], v[12:13], off
	v_add_co_u32_e32 v16, vcc, s42, v16
	s_nop 0
	v_addc_co_u32_e32 v17, vcc, 0, v17, vcc
	global_load_dwordx4 v[16:19], v[16:17], off
	s_nop 0
	global_load_dwordx4 v[20:23], v[52:53], off offset:16
	global_load_dwordx4 v[60:63], v[52:53], off
	global_load_dwordx4 v[24:27], v[54:55], off offset:16
	global_load_dwordx4 v[64:67], v[54:55], off
	s_waitcnt vmcnt(8)
	v_lshlrev_b32_e32 v68, 16, v0
	v_and_b32_e32 v69, 0xffff0000, v0
	v_mul_f32_e32 v0, 0x3d372713, v68
	s_waitcnt vmcnt(7)
	v_lshlrev_b32_e32 v70, 16, v4
	v_and_b32_e32 v71, 0xffff0000, v4
	v_mul_f32_e32 v0, v0, v68
	v_mov_b32_e32 v4, v68
	v_fmac_f32_e32 v4, v0, v4
	v_mul_f32_e32 v0, 0x3f4c422a, v4
	v_add_f32_e32 v0, v0, v0
	v_mul_f32_e32 v0, 0x3fb8aa3b, v0
	v_exp_f32_e32 v0, v0
	s_waitcnt vmcnt(6)
	v_lshlrev_b32_e32 v80, 16, v8
	v_and_b32_e32 v81, 0xffff0000, v8
	v_lshlrev_b32_e32 v4, 16, v5
	v_add_f32_e32 v0, 1.0, v0
	v_and_b32_e32 v5, 0xffff0000, v5
	v_lshlrev_b32_e32 v8, 16, v9
	v_and_b32_e32 v9, 0xffff0000, v9
	s_waitcnt vmcnt(5)
	v_lshlrev_b32_e32 v82, 16, v12
	v_and_b32_e32 v83, 0xffff0000, v12
	s_waitcnt vmcnt(4)
	v_lshlrev_b32_e32 v84, 16, v16
	v_and_b32_e32 v85, 0xffff0000, v16
	s_waitcnt vmcnt(2)
	v_pk_fma_f32 v[60:61], v[60:61], v[80:81], v[70:71]
	v_pk_mul_f32 v[70:71], v[68:69], 0.5 op_sel_hi:[1,0]
	v_pk_add_f32 v[60:61], v[60:61], v[82:83]
	v_lshlrev_b32_e32 v12, 16, v13
	s_waitcnt vmcnt(0)
	v_pk_fma_f32 v[60:61], v[64:65], v[84:85], v[60:61]
	v_rcp_f32_e32 v64, v0
	v_mul_f32_e32 v0, 0x3d372713, v69
	v_mul_f32_e32 v0, v0, v69
	v_fmac_f32_e32 v69, v0, v69
	v_mul_f32_e32 v0, 0x3f4c422a, v69
	v_add_f32_e32 v0, v0, v0
	v_mul_f32_e32 v0, 0x3fb8aa3b, v0
	v_exp_f32_e32 v0, v0
	v_and_b32_e32 v13, 0xffff0000, v13
	v_pk_fma_f32 v[4:5], v[62:63], v[8:9], v[4:5]
	v_lshlrev_b32_e32 v16, 16, v17
	v_add_f32_e32 v0, 1.0, v0
	v_rcp_f32_e32 v65, v0
	v_lshlrev_b32_e32 v0, 16, v1
	v_and_b32_e32 v1, 0xffff0000, v1
	v_mul_f32_e32 v8, 0x3d372713, v0
	v_pk_add_f32 v[4:5], v[4:5], v[12:13]
	v_mul_f32_e32 v8, v8, v0
	v_mov_b32_e32 v9, v0
	v_pk_mul_f32 v[12:13], v[0:1], 0.5 op_sel_hi:[1,0]
	v_mul_f32_e32 v0, 0x3d372713, v1
	v_mul_f32_e32 v0, v0, v1
	v_fmac_f32_e32 v9, v8, v9
	v_fmac_f32_e32 v1, v0, v1
	v_mul_f32_e32 v8, 0x3f4c422a, v9
	v_mul_f32_e32 v0, 0x3f4c422a, v1
	v_add_f32_e32 v8, v8, v8
	v_add_f32_e32 v0, v0, v0
	v_mul_f32_e32 v8, 0x3fb8aa3b, v8
	v_mul_f32_e32 v0, 0x3fb8aa3b, v0
	v_exp_f32_e32 v8, v8
	v_exp_f32_e32 v0, v0
	v_and_b32_e32 v17, 0xffff0000, v17
	v_pk_fma_f32 v[4:5], v[66:67], v[16:17], v[4:5]
	v_add_f32_e32 v8, 1.0, v8
	v_add_f32_e32 v0, 1.0, v0
	v_rcp_f32_e32 v8, v8
	v_rcp_f32_e32 v9, v0
	v_lshlrev_b32_e32 v16, 16, v14
	v_and_b32_e32 v17, 0xffff0000, v14
	v_lshlrev_b32_e32 v62, 16, v18
	v_pk_fma_f32 v[0:1], v[8:9], 2.0, 1.0 op_sel_hi:[1,0,0] neg_lo:[1,0,0] neg_hi:[1,0,0]
	v_lshlrev_b32_e32 v8, 16, v6
	v_pk_add_f32 v[0:1], v[0:1], 1.0 op_sel_hi:[1,0]
	v_and_b32_e32 v9, 0xffff0000, v6
	v_pk_mul_f32 v[0:1], v[12:13], v[0:1]
	v_lshlrev_b32_e32 v12, 16, v10
	v_pk_mul_f32 v[0:1], v[4:5], v[0:1]
	v_lshlrev_b32_e32 v4, 16, v2
	v_and_b32_e32 v5, 0xffff0000, v2
	v_mul_f32_e32 v2, 0x3d372713, v4
	v_mul_f32_e32 v2, v2, v4
	v_mov_b32_e32 v6, v4
	v_fmac_f32_e32 v6, v2, v6
	v_mul_f32_e32 v2, 0x3f4c422a, v6
	v_add_f32_e32 v2, v2, v2
	v_mul_f32_e32 v2, 0x3fb8aa3b, v2
	v_exp_f32_e32 v2, v2
	v_and_b32_e32 v13, 0xffff0000, v10
	v_pk_fma_f32 v[8:9], v[20:21], v[12:13], v[8:9]
	v_and_b32_e32 v63, 0xffff0000, v18
	v_add_f32_e32 v2, 1.0, v2
	v_rcp_f32_e32 v12, v2
	v_mul_f32_e32 v2, 0x3d372713, v5
	v_mul_f32_e32 v2, v2, v5
	v_pk_add_f32 v[8:9], v[8:9], v[16:17]
	v_pk_mul_f32 v[16:17], v[4:5], 0.5 op_sel_hi:[1,0]
	v_fmac_f32_e32 v5, v2, v5
	v_mul_f32_e32 v2, 0x3f4c422a, v5
	v_add_f32_e32 v2, v2, v2
	v_mul_f32_e32 v2, 0x3fb8aa3b, v2
	v_exp_f32_e32 v2, v2
	v_pk_fma_f32 v[8:9], v[24:25], v[62:63], v[8:9]
	v_lshlrev_b32_e32 v6, 16, v7
	v_and_b32_e32 v7, 0xffff0000, v7
	v_add_f32_e32 v2, 1.0, v2
	v_rcp_f32_e32 v13, v2
	v_lshlrev_b32_e32 v2, 16, v3
	v_and_b32_e32 v3, 0xffff0000, v3
	v_lshlrev_b32_e32 v10, 16, v15
	v_pk_fma_f32 v[4:5], v[12:13], 2.0, 1.0 op_sel_hi:[1,0,0] neg_lo:[1,0,0] neg_hi:[1,0,0]
	v_pk_fma_f32 v[64:65], v[64:65], 2.0, 1.0 op_sel_hi:[1,0,0] neg_lo:[1,0,0] neg_hi:[1,0,0]
	v_pk_add_f32 v[4:5], v[4:5], 1.0 op_sel_hi:[1,0]
	v_pk_add_f32 v[64:65], v[64:65], 1.0 op_sel_hi:[1,0]
	v_pk_mul_f32 v[4:5], v[16:17], v[4:5]
	v_lshlrev_b32_e32 v12, 16, v19
	v_pk_mul_f32 v[4:5], v[8:9], v[4:5]
	v_lshlrev_b32_e32 v8, 16, v11
	v_and_b32_e32 v9, 0xffff0000, v11
	v_and_b32_e32 v11, 0xffff0000, v15
	v_pk_fma_f32 v[6:7], v[22:23], v[8:9], v[6:7]
	v_mul_f32_e32 v8, 0x3d372713, v2
	v_pk_add_f32 v[6:7], v[6:7], v[10:11]
	v_mul_f32_e32 v8, v8, v2
	v_mov_b32_e32 v9, v2
	v_pk_mul_f32 v[10:11], v[2:3], 0.5 op_sel_hi:[1,0]
	v_mul_f32_e32 v2, 0x3d372713, v3
	v_mul_f32_e32 v2, v2, v3
	v_fmac_f32_e32 v9, v8, v9
	v_fmac_f32_e32 v3, v2, v3
	v_mul_f32_e32 v8, 0x3f4c422a, v9
	v_mul_f32_e32 v2, 0x3f4c422a, v3
	v_add_f32_e32 v8, v8, v8
	v_add_f32_e32 v2, v2, v2
	v_mul_f32_e32 v8, 0x3fb8aa3b, v8
	v_mul_f32_e32 v2, 0x3fb8aa3b, v2
	v_exp_f32_e32 v8, v8
	v_exp_f32_e32 v2, v2
	v_and_b32_e32 v13, 0xffff0000, v19
	v_pk_mul_f32 v[64:65], v[70:71], v[64:65]
	v_add_f32_e32 v8, 1.0, v8
	v_add_f32_e32 v2, 1.0, v2
	v_rcp_f32_e32 v8, v8
	v_rcp_f32_e32 v9, v2
	v_pk_fma_f32 v[6:7], v[26:27], v[12:13], v[6:7]
	v_pk_mul_f32 v[60:61], v[60:61], v[64:65]
	v_pk_fma_f32 v[2:3], v[8:9], 2.0, 1.0 op_sel_hi:[1,0,0] neg_lo:[1,0,0] neg_hi:[1,0,0]
	s_nop 0
	v_pk_add_f32 v[2:3], v[2:3], 1.0 op_sel_hi:[1,0]
	s_nop 0
	v_pk_mul_f32 v[2:3], v[10:11], v[2:3]
	s_nop 0
	v_pk_mul_f32 v[2:3], v[6:7], v[2:3]
	s_branch .LBB0_639
